# post pass: gain pointers via scalar loads instead of a dependent vector pointer fetch; Hyena skip gain requested before the main loop
# baseline (speedup 1.0000x reference)
.LBB0_766:
	s_mul_i32 s6, s73, 10
	s_add_i32 s46, s6, 3
	s_movk_i32 s6, 0x48
	s_ashr_i32 s7, s6, 31
	s_lshl_b64 s[6:7], s[6:7], 2
	s_add_u32 s6, s0, s6
	s_addc_u32 s7, s1, s7
	s_load_dwordx2 s[8:9], s[6:7], 0x0
	s_waitcnt lgkmcnt(0)
	s_cmp_le_i32 s8, s46
	s_cselect_b64 s[6:7], -1, 0
	s_cmp_lt_i32 s46, s9
	s_cselect_b64 s[8:9], -1, 0
	s_and_b64 s[6:7], s[6:7], s[8:9]
	s_andn2_b64 vcc, exec, s[6:7]
	s_cbranch_vccnz .LBB0_922
	s_waitcnt vmcnt(0)
	v_mbcnt_lo_u32_b32 v18, -1, 0
	v_mbcnt_hi_u32_b32 v18, -1, v18
	s_getreg_b32 s6, hwreg(HW_REG_HW_ID, 0, 6)
	s_lshl_b32 s6, s6, 2
	s_and_b32 s6, s6, 0xfc
	s_or_b32 s6, s6, 0x27100
	v_mov_b32_e32 v0, s6
	s_mov_b32 s6, 35
	ds_read_b32 v0, v0
	s_ashr_i32 s7, s6, 31
	s_lshl_b64 s[6:7], s[6:7], 3
	s_add_u32 s6, s0, s6
	s_addc_u32 s7, s1, s7
	s_load_dwordx2 s[20:21], s[6:7], 0x0
	v_bfe_u32 v52, v18, 2, 4
	s_waitcnt lgkmcnt(0)
	v_readfirstlane_b32 s8, v0
	v_cmp_lt_u32_e32 vcc, 5, v52
	s_load_dwordx2 s[10:11], s[0:1], 0xa8
	s_load_dwordx2 s[12:13], s[0:1], 0xb0
	s_waitcnt lgkmcnt(0)
	v_mov_b32_e32 v2, s10
	v_mov_b32_e32 v3, s11
	v_mov_b32_e32 v4, s12
	v_mov_b32_e32 v5, s13
	v_cndmask_b32_e32 v2, v2, v4, vcc
	v_cndmask_b32_e32 v3, v3, v5, vcc
	v_and_b32_e32 v19, 3, v18
	s_lshl_b32 s70, s73, 6
	v_lshlrev_b32_e32 v0, 6, v19
	s_mov_b32 s6, 35
	v_lshl_or_b32 v54, s8, 6, v18
	v_ashrrev_i32_e32 v55, 31, v54
	s_waitcnt vmcnt(0)
	v_lshl_add_u64 v[2:3], s[70:71], 2, v[2:3]
	v_lshl_add_u64 v[14:15], v[2:3], 0, v[0:1]
	global_load_dwordx4 v[2:5], v[14:15], off offset:48
	global_load_dwordx4 v[6:9], v[14:15], off offset:32
	global_load_dwordx4 v[10:13], v[14:15], off offset:16
	s_nop 0
	global_load_dwordx4 v[14:17], v[14:15], off
	s_barrier
	s_ashr_i32 s7, s6, 31
	s_lshl_b64 s[6:7], s[6:7], 3
	s_add_u32 s6, s0, s6
	s_addc_u32 s7, s1, s7
	s_load_dwordx2 s[6:7], s[6:7], 0x0
	v_lshl_add_u32 v0, v54, 4, 0
	s_waitcnt lgkmcnt(0)
	v_lshl_add_u64 v[20:21], v[54:55], 4, s[6:7]
	s_mov_b32 s6, 0x600000
	v_add_co_u32_e32 v20, vcc, s6, v20
	v_readlane_b32 s6, v254, 12
	s_nop 0
	v_addc_co_u32_e32 v21, vcc, 0, v21, vcc
	global_load_dwordx4 v[20:23], v[20:21], off
	s_waitcnt vmcnt(0)
	ds_write_b128 v0, v[20:23]
	v_ashrrev_i32_e32 v0, 5, v54
	v_and_b32_e32 v0, -2, v0
	v_add_u32_e32 v26, s6, v0
	s_mov_b32 s6, 0x8800
	v_cmp_gt_i32_e32 vcc, s6, v26
	s_waitcnt lgkmcnt(0)
	s_barrier
	s_and_saveexec_b64 s[22:23], vcc
	s_cbranch_execz .LBB0_806
	v_cmp_gt_u32_e64 s[6:7], 8, v52
	v_mov_b32_e32 v0, 0x380
	v_mov_b32_e32 v20, 0x300
	v_cndmask_b32_e64 v0, v0, v20, s[6:7]
	v_lshlrev_b32_e32 v22, 6, v52
	v_and_b32_e32 v18, 1, v18
	v_ashrrev_i32_e32 v27, 31, v26
	v_cmp_eq_u32_e64 s[10:11], 0, v18
	v_lshlrev_b64 v[20:21], 12, v[26:27]
	v_lshlrev_b32_e32 v18, 5, v19
	v_add_lshl_u32 v0, v0, v22, 1
	v_or3_b32 v20, v20, v18, v0
	v_lshlrev_b32_e32 v53, 4, v19
	v_cmp_gt_u32_e64 s[8:9], 2, v19
	v_cmp_lt_u32_e32 vcc, 13, v52
	v_lshl_add_u64 v[18:19], s[20:21], 0, v[20:21]
	s_mov_b64 s[12:13], 0x27801010
	v_cndmask_b32_e64 v55, 0, 8, vcc
	v_bfe_u32 v56, v54, 2, 1
	v_lshl_add_u64 v[28:29], v[18:19], 0, s[12:13]
	s_mov_b64 s[24:25], 0
	s_branch .LBB0_774

.LBB0_927:
	s_mov_b32 s8, 20
	s_ashr_i32 s9, s8, 31
	s_lshl_b64 s[8:9], s[8:9], 3
	s_add_u32 s8, s0, s8
	s_addc_u32 s9, s1, s9
	s_load_dwordx2 s[8:9], s[8:9], 0x0
	s_lshl_b64 s[6:7], s[6:7], 2
	v_lshlrev_b32_e32 v0, 3, v173
	v_or_b32_e32 v70, s18, v177
	v_and_b32_e32 v0, 16, v0
	s_waitcnt lgkmcnt(0)
	s_add_u32 s6, s8, s6
	s_addc_u32 s7, s9, s7
	s_mov_b32 s6, 35
	s_ashr_i32 s7, s6, 31
	s_lshl_b64 s[6:7], s[6:7], 3
	s_add_u32 s6, s0, s6
	s_addc_u32 s7, s1, s7
	s_load_dwordx2 s[6:7], s[6:7], 0x0
	s_waitcnt vmcnt(4)
	v_lshlrev_b32_e32 v74, 16, v170
	v_and_b32_e32 v75, 0xffff0000, v170
	v_and_b32_e32 v78, 16, v176
	s_add_i32 s17, s17, s3
	s_waitcnt lgkmcnt(0)
	v_lshl_add_u64 v[68:69], v[174:175], 1, s[6:7]
	s_add_i32 s6, 0, 0x10100
	v_add_u32_e32 v3, s6, v178
	v_lshl_add_u64 v[68:69], v[68:69], 0, v[0:1]
	v_lshlrev_b32_e32 v0, 7, v70
	v_lshlrev_b32_e32 v70, 6, v70
	v_add3_u32 v3, v3, v172, v0
	v_ashrrev_i32_e32 v71, 31, v70
	v_lshl_add_u64 v[72:73], v[70:71], 1, v[68:69]
	ds_read2_b64 v[68:71], v3 offset1:4
	v_lshlrev_b32_e32 v0, 1, v78
	s_mov_b64 s[6:7], 0x34400000
	s_cmpk_gt_i32 s17, 0xff
	s_waitcnt lgkmcnt(0)
	v_lshlrev_b32_e32 v76, 16, v68
	v_and_b32_e32 v77, 0xffff0000, v68
	v_lshlrev_b32_e32 v68, 16, v69
	v_and_b32_e32 v69, 0xffff0000, v69
	s_waitcnt vmcnt(0)
	v_mov_b32_e32 v2, v185
	v_pk_fma_f32 v[64:65], v[2:3], v[76:77], v[64:65] op_sel_hi:[0,1,1]
	v_pk_mul_f32 v[64:65], v[64:65], v[74:75]
	v_lshlrev_b32_e32 v74, 16, v171
	v_and_b32_e32 v75, 0xffff0000, v171
	v_pk_fma_f32 v[66:67], v[2:3], v[68:69], v[66:67] op_sel_hi:[0,1,1]
	v_pk_mul_f32 v[66:67], v[66:67], v[74:75]
	v_lshlrev_b32_e32 v68, 16, v70
	v_and_b32_e32 v69, 0xffff0000, v70
	v_cvt_pk_bf16_f32 v64, v64, v65
	v_cvt_pk_bf16_f32 v65, v66, v67
	v_lshlrev_b32_e32 v66, 16, v168
	v_and_b32_e32 v67, 0xffff0000, v168
	v_pk_fma_f32 v[60:61], v[2:3], v[68:69], v[60:61] op_sel_hi:[0,1,1]
	v_pk_mul_f32 v[60:61], v[60:61], v[66:67]
	v_lshlrev_b32_e32 v68, 16, v71
	v_and_b32_e32 v69, 0xffff0000, v71
	v_cvt_pk_bf16_f32 v66, v60, v61
	v_lshlrev_b32_e32 v60, 16, v169
	v_and_b32_e32 v61, 0xffff0000, v169
	v_pk_fma_f32 v[62:63], v[2:3], v[68:69], v[62:63] op_sel_hi:[0,1,1]
	v_pk_mul_f32 v[60:61], v[62:63], v[60:61]
	v_lshl_add_u64 v[62:63], v[72:73], 0, v[0:1]
	v_cvt_pk_bf16_f32 v67, v60, v61
	v_lshl_add_u64 v[60:61], v[62:63], 0, s[6:7]
	v_add_co_u32_e32 v62, vcc, s83, v62
	s_nop 1
	v_permlane16_swap_b32 v64, v66
	s_nop 1
	v_permlane16_swap_b32 v65, v67
	s_nop 1
	v_addc_co_u32_e32 v63, vcc, 0, v63, vcc
	global_store_dwordx4 v[62:63], v[64:67], off
	ds_read2_b64 v[62:65], v3 offset0:8 offset1:12
	s_waitcnt lgkmcnt(0)
	v_lshlrev_b32_e32 v68, 16, v62
	v_and_b32_e32 v69, 0xffff0000, v62
	v_lshlrev_b32_e32 v66, 16, v166
	v_and_b32_e32 v67, 0xffff0000, v166
	v_pk_fma_f32 v[56:57], v[2:3], v[68:69], v[56:57] op_sel_hi:[0,1,1]
	v_lshlrev_b32_e32 v62, 16, v63
	v_and_b32_e32 v63, 0xffff0000, v63
	v_pk_mul_f32 v[56:57], v[56:57], v[66:67]
	v_lshlrev_b32_e32 v66, 16, v167
	v_and_b32_e32 v67, 0xffff0000, v167
	v_pk_fma_f32 v[58:59], v[2:3], v[62:63], v[58:59] op_sel_hi:[0,1,1]
	v_pk_mul_f32 v[58:59], v[58:59], v[66:67]
	v_lshlrev_b32_e32 v62, 16, v64
	v_and_b32_e32 v63, 0xffff0000, v64
	v_cvt_pk_bf16_f32 v56, v56, v57
	v_cvt_pk_bf16_f32 v57, v58, v59
	v_lshlrev_b32_e32 v58, 16, v164
	v_and_b32_e32 v59, 0xffff0000, v164
	v_pk_fma_f32 v[52:53], v[2:3], v[62:63], v[52:53] op_sel_hi:[0,1,1]
	v_pk_mul_f32 v[52:53], v[52:53], v[58:59]
	v_lshlrev_b32_e32 v62, 16, v65
	v_and_b32_e32 v63, 0xffff0000, v65
	v_cvt_pk_bf16_f32 v58, v52, v53
	v_lshlrev_b32_e32 v52, 16, v165
	v_and_b32_e32 v53, 0xffff0000, v165
	v_pk_fma_f32 v[54:55], v[2:3], v[62:63], v[54:55] op_sel_hi:[0,1,1]
	v_pk_mul_f32 v[52:53], v[54:55], v[52:53]
	s_nop 1
	v_permlane16_swap_b32 v56, v58
	s_nop 0
	v_cvt_pk_bf16_f32 v59, v52, v53
	s_nop 1
	v_permlane16_swap_b32 v57, v59
	global_store_dwordx4 v[60:61], v[56:59], off offset:64
	ds_read2_b64 v[54:57], v3 offset0:32 offset1:36
	v_lshlrev_b32_e32 v52, 16, v162
	v_and_b32_e32 v53, 0xffff0000, v162
	s_waitcnt lgkmcnt(0)
	v_lshlrev_b32_e32 v58, 16, v54
	v_and_b32_e32 v59, 0xffff0000, v54
	v_pk_fma_f32 v[48:49], v[2:3], v[58:59], v[48:49] op_sel_hi:[0,1,1]
	v_lshlrev_b32_e32 v54, 16, v55
	v_and_b32_e32 v55, 0xffff0000, v55
	v_pk_mul_f32 v[48:49], v[48:49], v[52:53]
	v_lshlrev_b32_e32 v52, 16, v163
	v_and_b32_e32 v53, 0xffff0000, v163
	v_pk_fma_f32 v[50:51], v[2:3], v[54:55], v[50:51] op_sel_hi:[0,1,1]
	v_pk_mul_f32 v[50:51], v[50:51], v[52:53]
	v_lshlrev_b32_e32 v52, 16, v56
	v_and_b32_e32 v53, 0xffff0000, v56
	v_cvt_pk_bf16_f32 v48, v48, v49
	v_cvt_pk_bf16_f32 v49, v50, v51
	v_lshlrev_b32_e32 v50, 16, v160
	v_and_b32_e32 v51, 0xffff0000, v160
	v_pk_fma_f32 v[44:45], v[2:3], v[52:53], v[44:45] op_sel_hi:[0,1,1]
	v_pk_mul_f32 v[44:45], v[44:45], v[50:51]
	v_lshlrev_b32_e32 v52, 16, v57
	v_and_b32_e32 v53, 0xffff0000, v57
	v_cvt_pk_bf16_f32 v50, v44, v45
	v_lshlrev_b32_e32 v44, 16, v161
	v_and_b32_e32 v45, 0xffff0000, v161
	v_pk_fma_f32 v[46:47], v[2:3], v[52:53], v[46:47] op_sel_hi:[0,1,1]
	v_pk_mul_f32 v[44:45], v[46:47], v[44:45]
	s_nop 1
	v_permlane16_swap_b32 v48, v50
	s_nop 0
	v_cvt_pk_bf16_f32 v51, v44, v45
	s_nop 1
	v_permlane16_swap_b32 v49, v51
	ds_read2_b64 v[44:47], v3 offset0:40 offset1:44
	global_store_dwordx4 v[60:61], v[48:51], off offset:256
	s_nop 1
	v_lshlrev_b32_e32 v48, 16, v158
	s_waitcnt lgkmcnt(0)
	v_lshlrev_b32_e32 v50, 16, v44
	v_and_b32_e32 v51, 0xffff0000, v44
	v_and_b32_e32 v49, 0xffff0000, v158
	v_pk_fma_f32 v[40:41], v[2:3], v[50:51], v[40:41] op_sel_hi:[0,1,1]
	v_lshlrev_b32_e32 v44, 16, v45
	v_and_b32_e32 v45, 0xffff0000, v45
	v_pk_mul_f32 v[40:41], v[40:41], v[48:49]
	v_lshlrev_b32_e32 v48, 16, v159
	v_and_b32_e32 v49, 0xffff0000, v159
	v_pk_fma_f32 v[42:43], v[2:3], v[44:45], v[42:43] op_sel_hi:[0,1,1]
	v_pk_mul_f32 v[42:43], v[42:43], v[48:49]
	v_lshlrev_b32_e32 v44, 16, v46
	v_and_b32_e32 v45, 0xffff0000, v46
	v_cvt_pk_bf16_f32 v40, v40, v41
	v_cvt_pk_bf16_f32 v41, v42, v43
	v_lshlrev_b32_e32 v42, 16, v156
	v_and_b32_e32 v43, 0xffff0000, v156
	v_pk_fma_f32 v[36:37], v[2:3], v[44:45], v[36:37] op_sel_hi:[0,1,1]
	v_pk_mul_f32 v[36:37], v[36:37], v[42:43]
	v_lshlrev_b32_e32 v44, 16, v47
	v_and_b32_e32 v45, 0xffff0000, v47
	v_cvt_pk_bf16_f32 v42, v36, v37
	v_lshlrev_b32_e32 v36, 16, v157
	v_and_b32_e32 v37, 0xffff0000, v157
	v_pk_fma_f32 v[38:39], v[2:3], v[44:45], v[38:39] op_sel_hi:[0,1,1]
	v_pk_mul_f32 v[36:37], v[38:39], v[36:37]
	s_nop 1
	v_permlane16_swap_b32 v40, v42
	s_nop 0
	v_cvt_pk_bf16_f32 v43, v36, v37
	s_nop 1
	v_permlane16_swap_b32 v41, v43
	ds_read2_b64 v[36:39], v3 offset0:64 offset1:68
	global_store_dwordx4 v[60:61], v[40:43], off offset:320
	s_nop 1
	v_lshlrev_b32_e32 v40, 16, v154
	s_waitcnt lgkmcnt(0)
	v_lshlrev_b32_e32 v42, 16, v36
	v_and_b32_e32 v43, 0xffff0000, v36
	v_and_b32_e32 v41, 0xffff0000, v154
	v_pk_fma_f32 v[32:33], v[2:3], v[42:43], v[32:33] op_sel_hi:[0,1,1]
	v_lshlrev_b32_e32 v36, 16, v37
	v_and_b32_e32 v37, 0xffff0000, v37
	v_pk_mul_f32 v[32:33], v[32:33], v[40:41]
	v_lshlrev_b32_e32 v40, 16, v155
	v_and_b32_e32 v41, 0xffff0000, v155
	v_pk_fma_f32 v[34:35], v[2:3], v[36:37], v[34:35] op_sel_hi:[0,1,1]
	v_pk_mul_f32 v[34:35], v[34:35], v[40:41]
	v_lshlrev_b32_e32 v36, 16, v38
	v_and_b32_e32 v37, 0xffff0000, v38
	v_cvt_pk_bf16_f32 v32, v32, v33
	v_cvt_pk_bf16_f32 v33, v34, v35
	v_lshlrev_b32_e32 v34, 16, v152
	v_and_b32_e32 v35, 0xffff0000, v152
	v_pk_fma_f32 v[28:29], v[2:3], v[36:37], v[28:29] op_sel_hi:[0,1,1]
	v_pk_mul_f32 v[28:29], v[28:29], v[34:35]
	v_lshlrev_b32_e32 v36, 16, v39
	v_and_b32_e32 v37, 0xffff0000, v39
	v_cvt_pk_bf16_f32 v34, v28, v29
	v_lshlrev_b32_e32 v28, 16, v153
	v_and_b32_e32 v29, 0xffff0000, v153
	v_pk_fma_f32 v[30:31], v[2:3], v[36:37], v[30:31] op_sel_hi:[0,1,1]
	v_pk_mul_f32 v[28:29], v[30:31], v[28:29]
	s_nop 1
	v_permlane16_swap_b32 v32, v34
	s_nop 0
	v_cvt_pk_bf16_f32 v35, v28, v29
	s_nop 1
	v_permlane16_swap_b32 v33, v35
	ds_read2_b64 v[28:31], v3 offset0:72 offset1:76
	global_store_dwordx4 v[60:61], v[32:35], off offset:512
	s_nop 1
	v_lshlrev_b32_e32 v32, 16, v150
	s_waitcnt lgkmcnt(0)
	v_lshlrev_b32_e32 v34, 16, v28
	v_and_b32_e32 v35, 0xffff0000, v28
	v_and_b32_e32 v33, 0xffff0000, v150
	v_pk_fma_f32 v[24:25], v[2:3], v[34:35], v[24:25] op_sel_hi:[0,1,1]
	v_lshlrev_b32_e32 v28, 16, v29
	v_and_b32_e32 v29, 0xffff0000, v29
	v_pk_mul_f32 v[24:25], v[24:25], v[32:33]
	v_lshlrev_b32_e32 v32, 16, v151
	v_and_b32_e32 v33, 0xffff0000, v151
	v_pk_fma_f32 v[26:27], v[2:3], v[28:29], v[26:27] op_sel_hi:[0,1,1]
	v_pk_mul_f32 v[26:27], v[26:27], v[32:33]
	v_lshlrev_b32_e32 v28, 16, v30
	v_and_b32_e32 v29, 0xffff0000, v30
	v_cvt_pk_bf16_f32 v24, v24, v25
	v_cvt_pk_bf16_f32 v25, v26, v27
	v_lshlrev_b32_e32 v26, 16, v148
	v_and_b32_e32 v27, 0xffff0000, v148
	v_pk_fma_f32 v[20:21], v[2:3], v[28:29], v[20:21] op_sel_hi:[0,1,1]
	v_pk_mul_f32 v[20:21], v[20:21], v[26:27]
	v_lshlrev_b32_e32 v28, 16, v31
	v_and_b32_e32 v29, 0xffff0000, v31
	v_cvt_pk_bf16_f32 v26, v20, v21
	v_lshlrev_b32_e32 v20, 16, v149
	v_and_b32_e32 v21, 0xffff0000, v149
	v_pk_fma_f32 v[22:23], v[2:3], v[28:29], v[22:23] op_sel_hi:[0,1,1]
	v_pk_mul_f32 v[20:21], v[22:23], v[20:21]
	s_nop 1
	v_permlane16_swap_b32 v24, v26
	s_nop 0
	v_cvt_pk_bf16_f32 v27, v20, v21
	s_nop 1
	v_permlane16_swap_b32 v25, v27
	ds_read2_b64 v[20:23], v3 offset0:96 offset1:100
	global_store_dwordx4 v[60:61], v[24:27], off offset:576
	s_nop 1
	v_lshlrev_b32_e32 v24, 16, v146
	s_waitcnt lgkmcnt(0)
	v_lshlrev_b32_e32 v26, 16, v20
	v_and_b32_e32 v27, 0xffff0000, v20
	v_and_b32_e32 v25, 0xffff0000, v146
	v_pk_fma_f32 v[16:17], v[2:3], v[26:27], v[16:17] op_sel_hi:[0,1,1]
	v_lshlrev_b32_e32 v20, 16, v21
	v_and_b32_e32 v21, 0xffff0000, v21
	v_pk_mul_f32 v[16:17], v[16:17], v[24:25]
	v_lshlrev_b32_e32 v24, 16, v147
	v_and_b32_e32 v25, 0xffff0000, v147
	v_pk_fma_f32 v[18:19], v[2:3], v[20:21], v[18:19] op_sel_hi:[0,1,1]
	v_pk_mul_f32 v[18:19], v[18:19], v[24:25]
	v_lshlrev_b32_e32 v20, 16, v22
	v_and_b32_e32 v21, 0xffff0000, v22
	v_cvt_pk_bf16_f32 v16, v16, v17
	v_cvt_pk_bf16_f32 v17, v18, v19
	v_lshlrev_b32_e32 v18, 16, v144
	v_and_b32_e32 v19, 0xffff0000, v144
	v_pk_fma_f32 v[12:13], v[2:3], v[20:21], v[12:13] op_sel_hi:[0,1,1]
	v_pk_mul_f32 v[12:13], v[12:13], v[18:19]
	v_lshlrev_b32_e32 v20, 16, v23
	v_and_b32_e32 v21, 0xffff0000, v23
	v_cvt_pk_bf16_f32 v18, v12, v13
	v_lshlrev_b32_e32 v12, 16, v145
	v_and_b32_e32 v13, 0xffff0000, v145
	v_pk_fma_f32 v[14:15], v[2:3], v[20:21], v[14:15] op_sel_hi:[0,1,1]
	v_pk_mul_f32 v[12:13], v[14:15], v[12:13]
	s_nop 1
	v_permlane16_swap_b32 v16, v18
	s_nop 0
	v_cvt_pk_bf16_f32 v19, v12, v13
	s_nop 1
	v_permlane16_swap_b32 v17, v19
	ds_read2_b64 v[12:15], v3 offset0:104 offset1:108
	global_store_dwordx4 v[60:61], v[16:19], off offset:768
	s_nop 1
	v_lshlrev_b32_e32 v16, 16, v142
	s_waitcnt lgkmcnt(0)
	v_lshlrev_b32_e32 v18, 16, v12
	v_and_b32_e32 v19, 0xffff0000, v12
	v_and_b32_e32 v17, 0xffff0000, v142
	v_pk_fma_f32 v[8:9], v[2:3], v[18:19], v[8:9] op_sel_hi:[0,1,1]
	v_lshlrev_b32_e32 v12, 16, v13
	v_and_b32_e32 v13, 0xffff0000, v13
	v_pk_mul_f32 v[8:9], v[8:9], v[16:17]
	v_lshlrev_b32_e32 v16, 16, v143
	v_and_b32_e32 v17, 0xffff0000, v143
	v_pk_fma_f32 v[10:11], v[2:3], v[12:13], v[10:11] op_sel_hi:[0,1,1]
	v_pk_mul_f32 v[10:11], v[10:11], v[16:17]
	v_lshlrev_b32_e32 v12, 16, v14
	v_and_b32_e32 v13, 0xffff0000, v14
	v_cvt_pk_bf16_f32 v8, v8, v9
	v_cvt_pk_bf16_f32 v9, v10, v11
	v_lshlrev_b32_e32 v10, 16, v140
	v_and_b32_e32 v11, 0xffff0000, v140
	v_pk_fma_f32 v[4:5], v[2:3], v[12:13], v[4:5] op_sel_hi:[0,1,1]
	v_pk_mul_f32 v[4:5], v[4:5], v[10:11]
	v_lshlrev_b32_e32 v12, 16, v15
	v_and_b32_e32 v13, 0xffff0000, v15
	v_cvt_pk_bf16_f32 v10, v4, v5
	v_lshlrev_b32_e32 v4, 16, v141
	v_and_b32_e32 v5, 0xffff0000, v141
	v_pk_fma_f32 v[2:3], v[2:3], v[12:13], v[6:7] op_sel_hi:[0,1,1]
	v_pk_mul_f32 v[2:3], v[2:3], v[4:5]
	s_nop 1
	v_permlane16_swap_b32 v8, v10
	s_nop 0
	v_cvt_pk_bf16_f32 v11, v2, v3
	s_nop 1
	v_permlane16_swap_b32 v9, v11
	global_store_dwordx4 v[60:61], v[8:11], off offset:832
	s_barrier
	s_cbranch_scc1 .LBB0_970

.LBB0_935:
	s_mov_b32 s10, 35
	s_waitcnt lgkmcnt(0)
	s_barrier
	s_ashr_i32 s11, s10, 31
	s_ashr_i32 s12, s9, 6
	s_lshl_b64 s[10:11], s[10:11], 3
	s_add_u32 s10, s0, s10
	s_addc_u32 s11, s1, s11
	s_load_dwordx2 s[10:11], s[10:11], 0x0
	v_bfe_u32 v9, v176, 1, 3
	v_lshl_add_u32 v2, v9, 8, s8
	v_and_b32_e32 v177, 1, v176
	v_ashrrev_i32_e32 v3, 31, v2
	v_bfe_u32 v8, v0, 4, 2
	v_lshlrev_b64 v[4:5], 13, v[2:3]
	v_lshlrev_b32_e32 v6, 6, v177
	v_lshlrev_b32_e32 v172, 3, v8
	s_waitcnt lgkmcnt(0)
	v_lshl_add_u64 v[4:5], s[10:11], 0, v[4:5]
	v_mov_b32_e32 v173, v1
	v_lshl_or_b32 v6, s12, 9, v6
	v_lshl_add_u64 v[4:5], v[4:5], 0, v[172:173]
	v_ashrrev_i32_e32 v7, 31, v6
	v_lshl_add_u64 v[4:5], v[6:7], 1, v[4:5]
	s_mov_b64 s[8:9], 0x35400000
	v_lshl_add_u64 v[6:7], v[4:5], 0, s[8:9]
	s_mov_b32 s8, 0x35400000
	v_add_co_u32_e32 v4, vcc, s8, v4
	s_movk_i32 s8, 0xffc
	s_nop 0
	v_addc_co_u32_e32 v5, vcc, 0, v5, vcc
	global_load_dwordx2 v[168:169], v[6:7], off offset:32
	global_load_dwordx2 v[166:167], v[6:7], off offset:64
	global_load_dwordx2 v[164:165], v[6:7], off offset:96
	global_load_dwordx2 v[162:163], v[6:7], off offset:256
	global_load_dwordx2 v[160:161], v[6:7], off offset:288
	global_load_dwordx2 v[158:159], v[6:7], off offset:320
	global_load_dwordx2 v[156:157], v[6:7], off offset:352
	global_load_dwordx2 v[154:155], v[6:7], off offset:512
	global_load_dwordx2 v[152:153], v[6:7], off offset:544
	global_load_dwordx2 v[150:151], v[6:7], off offset:576
	global_load_dwordx2 v[148:149], v[6:7], off offset:608
	global_load_dwordx2 v[146:147], v[6:7], off offset:768
	global_load_dwordx2 v[170:171], v[4:5], off
	global_load_dwordx2 v[144:145], v[6:7], off offset:800
	global_load_dwordx2 v[142:143], v[6:7], off offset:832
	global_load_dwordx2 v[140:141], v[6:7], off offset:864
	s_load_dwordx2 s[14:15], s[0:1], 0xa0
	s_lshl_b64 vcc, s[6:7], 2
	s_waitcnt lgkmcnt(0)
	s_add_u32 s14, s14, vcc_lo
	s_addc_u32 s15, s15, vcc_hi
	global_load_dword v185, v1, s[14:15]
	v_and_b32_e32 v4, 15, v176
	v_mov_b32_e32 v5, 0xfff
	v_lshrrev_b32_e32 v173, 4, v0
	v_bitop3_b32 v0, v4, 3, v5 bitop3:0x48
	v_bitop3_b32 v4, v4, s8, v5 bitop3:0x48
	v_add_u32_e32 v4, v172, v4
	v_mul_u32_u24_e32 v178, 0x2020, v9
	v_lshlrev_b32_e32 v179, 4, v8
	v_lshlrev_b64 v[174:175], 12, v[2:3]
	v_mul_u32_u24_e32 v0, 0x4040, v0
	s_lshl_b32 s18, s12, 3
	s_sub_i32 s20, s18, 63
	v_lshl_add_u32 v180, v4, 1, v0
	s_lshl_b32 s8, s20, 7
	v_subrev_u32_e32 v0, s8, v180
	v_add_u32_e32 v0, 0, v0
	v_subrev_u32_e32 v2, 32, v0
	ds_read_b64 v[124:125], v0 offset:64
	ds_read_b64 v[126:127], v0 offset:72
	ds_read_b64 v[128:129], v0 offset:32
	ds_read_b64 v[130:131], v0 offset:40
	ds_read_b64 v[132:133], v0
	ds_read_b64 v[134:135], v0 offset:8
	ds_read_b64 v[136:137], v2
	v_subrev_u32_e32 v2, 24, v0
	ds_read_b64 v[138:139], v2
	v_subrev_u32_e32 v2, 64, v0
	ds_read_b64 v[68:69], v2
	v_subrev_u32_e32 v2, 56, v0
	ds_read_b64 v[70:71], v2
	v_add_u32_e32 v2, 0xffffffa0, v0
	v_add_u32_e32 v0, 0xffffffa8, v0
	ds_read_b64 v[72:73], v2
	ds_read_b64 v[74:75], v0
	v_lshlrev_b32_e32 v0, 7, v177
	s_movk_i32 s8, 0x2020
	v_mad_u32_u24 v0, v9, s8, v0
	s_mov_b32 s8, 0x12080
	v_mov_b32_e32 v2, v1
	v_mov_b32_e32 v3, v1
	v_add3_u32 v184, v0, v179, s8
	v_mov_b32_e32 v0, v1
	v_mov_b64_e32 v[6:7], v[2:3]
	v_mov_b64_e32 v[22:23], v[2:3]
	v_mov_b64_e32 v[38:39], v[2:3]
	v_mov_b64_e32 v[54:55], v[2:3]
	v_mov_b64_e32 v[10:11], v[2:3]
	v_mov_b64_e32 v[26:27], v[2:3]
	v_mov_b64_e32 v[42:43], v[2:3]
	v_mov_b64_e32 v[58:59], v[2:3]
	v_mov_b64_e32 v[14:15], v[2:3]
	v_mov_b64_e32 v[30:31], v[2:3]
	v_mov_b64_e32 v[46:47], v[2:3]
	v_mov_b64_e32 v[62:63], v[2:3]
	v_mov_b64_e32 v[18:19], v[2:3]
	v_mov_b64_e32 v[34:35], v[2:3]
	v_mov_b64_e32 v[50:51], v[2:3]
	v_mov_b64_e32 v[66:67], v[2:3]
	s_or_b32 s19, s18, 7
	v_subrev_u32_e32 v183, 32, v180
	v_subrev_u32_e32 v182, 64, v180
	v_add_u32_e32 v181, 0xffffffa0, v180
	s_movk_i32 s21, 0x46
	v_mov_b64_e32 v[4:5], v[0:1]
	v_mov_b64_e32 v[20:21], v[0:1]
	v_mov_b64_e32 v[36:37], v[0:1]
	v_mov_b64_e32 v[52:53], v[0:1]
	v_mov_b64_e32 v[8:9], v[0:1]
	v_mov_b64_e32 v[24:25], v[0:1]
	v_mov_b64_e32 v[40:41], v[0:1]
	v_mov_b64_e32 v[56:57], v[0:1]
	v_mov_b64_e32 v[12:13], v[0:1]
	v_mov_b64_e32 v[28:29], v[0:1]
	v_mov_b64_e32 v[44:45], v[0:1]
	v_mov_b64_e32 v[60:61], v[0:1]
	v_mov_b64_e32 v[16:17], v[0:1]
	v_mov_b64_e32 v[32:33], v[0:1]
	v_mov_b64_e32 v[48:49], v[0:1]
	v_mov_b64_e32 v[64:65], v[0:1]
